# speedup vs baseline: 1.0050x; 1.0013x over previous
.LBB1_84:
	s_or_b64 exec, exec, s[2:3]
	v_lshrrev_b32_e32 v20, 3, v0
	v_and_b32_e32 v1, 7, v0
	v_lshlrev_b32_e32 v1, 4, v1
	v_or_b32_e32 v24, s46, v20
	v_lshlrev_b32_e32 v20, 2, v20
	s_mov_b32 s2, 0x186a0
	s_waitcnt lgkmcnt(0)
	s_barrier
	ds_read_b32 v26, v20 offset:4220
	ds_read_b32 v28, v20 offset:4476
	ds_read_b32 v30, v20 offset:4732
	ds_read_b32 v32, v20 offset:4988
	v_cvt_f32_f16_e32 v2, v60
	v_cvt_f32_f16_sdwa v3, v60 dst_sel:DWORD dst_unused:UNUSED_PAD src0_sel:WORD_1
	v_cvt_f32_f16_e32 v4, v61
	v_cvt_f32_f16_sdwa v5, v61 dst_sel:DWORD dst_unused:UNUSED_PAD src0_sel:WORD_1
	v_cvt_f32_f16_e32 v6, v62
	v_cvt_f32_f16_sdwa v7, v62 dst_sel:DWORD dst_unused:UNUSED_PAD src0_sel:WORD_1
	v_cvt_f32_f16_e32 v8, v63
	v_cvt_f32_f16_sdwa v9, v63 dst_sel:DWORD dst_unused:UNUSED_PAD src0_sel:WORD_1
	v_add_u32_e32 v10, 0, v24
	s_waitcnt lgkmcnt(3)
	v_pk_mul_f32 v[2:3], v[26:27], v[2:3] op_sel_hi:[0,1]
	v_pk_mul_f32 v[4:5], v[26:27], v[4:5] op_sel_hi:[0,1]
	v_pk_mul_f32 v[6:7], v[26:27], v[6:7] op_sel_hi:[0,1]
	v_pk_mul_f32 v[8:9], v[26:27], v[8:9] op_sel_hi:[0,1]
	v_cmp_gt_u32_e32 vcc, s2, v10
	v_lshl_or_b32 v11, v10, 7, v1
	v_cvt_pk_f16_f32 v60, v2, v3
	v_cvt_pk_f16_f32 v61, v4, v5
	v_cvt_pk_f16_f32 v62, v6, v7
	v_cvt_pk_f16_f32 v63, v8, v9
	s_and_saveexec_b64 s[0:1], vcc
	global_store_dwordx4 v11, v[60:63], s[44:45] sc1
	s_or_b64 exec, exec, s[0:1]
	v_cvt_f32_f16_e32 v2, v64
	v_cvt_f32_f16_sdwa v3, v64 dst_sel:DWORD dst_unused:UNUSED_PAD src0_sel:WORD_1
	v_cvt_f32_f16_e32 v4, v65
	v_cvt_f32_f16_sdwa v5, v65 dst_sel:DWORD dst_unused:UNUSED_PAD src0_sel:WORD_1
	v_cvt_f32_f16_e32 v6, v66
	v_cvt_f32_f16_sdwa v7, v66 dst_sel:DWORD dst_unused:UNUSED_PAD src0_sel:WORD_1
	v_cvt_f32_f16_e32 v8, v67
	v_cvt_f32_f16_sdwa v9, v67 dst_sel:DWORD dst_unused:UNUSED_PAD src0_sel:WORD_1
	v_add_u32_e32 v10, 64, v24
	s_waitcnt lgkmcnt(2)
	v_pk_mul_f32 v[2:3], v[28:29], v[2:3] op_sel_hi:[0,1]
	v_pk_mul_f32 v[4:5], v[28:29], v[4:5] op_sel_hi:[0,1]
	v_pk_mul_f32 v[6:7], v[28:29], v[6:7] op_sel_hi:[0,1]
	v_pk_mul_f32 v[8:9], v[28:29], v[8:9] op_sel_hi:[0,1]
	v_cmp_gt_u32_e32 vcc, s2, v10
	v_lshl_or_b32 v11, v10, 7, v1
	v_cvt_pk_f16_f32 v64, v2, v3
	v_cvt_pk_f16_f32 v65, v4, v5
	v_cvt_pk_f16_f32 v66, v6, v7
	v_cvt_pk_f16_f32 v67, v8, v9
	s_and_saveexec_b64 s[0:1], vcc
	global_store_dwordx4 v11, v[64:67], s[44:45] sc1
	s_or_b64 exec, exec, s[0:1]
	v_cvt_f32_f16_e32 v2, v68
	v_cvt_f32_f16_sdwa v3, v68 dst_sel:DWORD dst_unused:UNUSED_PAD src0_sel:WORD_1
	v_cvt_f32_f16_e32 v4, v69
	v_cvt_f32_f16_sdwa v5, v69 dst_sel:DWORD dst_unused:UNUSED_PAD src0_sel:WORD_1
	v_cvt_f32_f16_e32 v6, v70
	v_cvt_f32_f16_sdwa v7, v70 dst_sel:DWORD dst_unused:UNUSED_PAD src0_sel:WORD_1
	v_cvt_f32_f16_e32 v8, v71
	v_cvt_f32_f16_sdwa v9, v71 dst_sel:DWORD dst_unused:UNUSED_PAD src0_sel:WORD_1
	v_add_u32_e32 v10, 0x80, v24
	s_waitcnt lgkmcnt(1)
	v_pk_mul_f32 v[2:3], v[30:31], v[2:3] op_sel_hi:[0,1]
	v_pk_mul_f32 v[4:5], v[30:31], v[4:5] op_sel_hi:[0,1]
	v_pk_mul_f32 v[6:7], v[30:31], v[6:7] op_sel_hi:[0,1]
	v_pk_mul_f32 v[8:9], v[30:31], v[8:9] op_sel_hi:[0,1]
	v_cmp_gt_u32_e32 vcc, s2, v10
	v_lshl_or_b32 v11, v10, 7, v1
	v_cvt_pk_f16_f32 v68, v2, v3
	v_cvt_pk_f16_f32 v69, v4, v5
	v_cvt_pk_f16_f32 v70, v6, v7
	v_cvt_pk_f16_f32 v71, v8, v9
	s_and_saveexec_b64 s[0:1], vcc
	global_store_dwordx4 v11, v[68:71], s[44:45] sc1
	s_or_b64 exec, exec, s[0:1]
	v_cvt_f32_f16_e32 v2, v56
	v_cvt_f32_f16_sdwa v3, v56 dst_sel:DWORD dst_unused:UNUSED_PAD src0_sel:WORD_1
	v_cvt_f32_f16_e32 v4, v57
	v_cvt_f32_f16_sdwa v5, v57 dst_sel:DWORD dst_unused:UNUSED_PAD src0_sel:WORD_1
	v_cvt_f32_f16_e32 v6, v58
	v_cvt_f32_f16_sdwa v7, v58 dst_sel:DWORD dst_unused:UNUSED_PAD src0_sel:WORD_1
	v_cvt_f32_f16_e32 v8, v59
	v_cvt_f32_f16_sdwa v9, v59 dst_sel:DWORD dst_unused:UNUSED_PAD src0_sel:WORD_1
	v_add_u32_e32 v10, 0xc0, v24
	s_waitcnt lgkmcnt(0)
	v_pk_mul_f32 v[2:3], v[32:33], v[2:3] op_sel_hi:[0,1]
	v_pk_mul_f32 v[4:5], v[32:33], v[4:5] op_sel_hi:[0,1]
	v_pk_mul_f32 v[6:7], v[32:33], v[6:7] op_sel_hi:[0,1]
	v_pk_mul_f32 v[8:9], v[32:33], v[8:9] op_sel_hi:[0,1]
	v_cmp_gt_u32_e32 vcc, s2, v10
	v_lshl_or_b32 v11, v10, 7, v1
	v_cvt_pk_f16_f32 v56, v2, v3
	v_cvt_pk_f16_f32 v57, v4, v5
	v_cvt_pk_f16_f32 v58, v6, v7
	v_cvt_pk_f16_f32 v59, v8, v9
	s_and_saveexec_b64 s[0:1], vcc
	global_store_dwordx4 v11, v[56:59], s[44:45] sc1
	s_or_b64 exec, exec, s[0:1]
	v_cmp_gt_i32_e32 vcc, s33, v0
	s_and_saveexec_b64 s[2:3], vcc
	s_cbranch_execz .LBB1_99
	v_not_b32_e32 v1, v0
	v_add_u32_e32 v2, s33, v1
	s_movk_i32 s4, 0x2a00
	s_movk_i32 s6, 0x29ff
	v_cmp_gt_u32_e64 s[4:5], s4, v2
	v_cmp_lt_u32_e32 vcc, s6, v2
	v_mov_b32_e32 v1, v0
	s_and_saveexec_b64 s[6:7], vcc
	s_cbranch_execz .LBB1_96
	s_add_i32 s8, s36, s38
	s_add_i32 s8, s8, s39
	s_add_i32 s8, s8, s40
	s_add_i32 s8, s8, s41
	s_add_i32 s8, s8, s42
	s_add_i32 s8, s8, s43
	s_add_i32 s8, s8, s37
	v_add_u32_e32 v1, s8, v0
	v_and_b32_e32 v3, 0xfffffe00, v2
	v_add_u32_e32 v3, v1, v3
	v_cmp_ge_i32_e32 vcc, v3, v1
	s_mov_b64 s[10:11], -1
	v_mov_b32_e32 v1, v0
	s_and_saveexec_b64 s[8:9], vcc
	s_cbranch_execz .LBB1_95
	v_lshrrev_b32_e32 v4, 9, v2
	v_add_u32_e32 v2, -1, v4
	v_or_b32_e32 v1, 0x200, v0
	v_lshrrev_b32_e32 v3, 1, v2
	s_mov_b32 s15, 0
	v_add_u32_e32 v5, 1, v3
	v_cmp_lt_u32_e32 vcc, 5, v2
	v_mov_b32_e32 v8, 0
	v_mov_b64_e32 v[2:3], v[0:1]
	s_and_saveexec_b64 s[10:11], vcc
	s_cbranch_execz .LBB1_91
	s_add_i32 s16, s34, 0x400
	s_add_i32 s18, s34, 0x800
	s_add_i32 s20, s34, 0xc00
	v_mov_b32_e32 v2, 0x2000
	v_and_b32_e32 v6, -4, v5
	s_mov_b32 s17, s16
	s_mov_b32 s19, s18
	s_mov_b32 s21, s20
	v_lshl_or_b32 v7, v0, 3, v2
	s_mov_b64 s[12:13], 0
	v_mov_b64_e32 v[2:3], v[0:1]

.LBB1_99:
	s_or_b64 exec, exec, s[2:3]
	s_endpgm
